# sc1 write-through on residual-GEMM epilogue stores (x tile + ss)
# speedup vs baseline: 1.0009x; 1.0009x over previous
; __device__ __forceinline__ unsigned cvt_pk_bf16(float lo, float hi) { const f32x2_t v = {lo, hi}; const bf16x2_t b = __builtin_convertvector(v, bf16x2_t); return __builtin_bit_cast(unsigned, b); }
; #define EPIRES_LOAD(buf, g) do { _Pragma("unroll") for (int bj = 0; bj < 2; ++bj) xb[buf][bj] = *(const u32x4*)(x + EPIRES_OFF(g, bj)); } while (0)
;     __device__ __forceinline__ void operator()(const f32x4 (&acc)[2][2][4][2], const Unit& u, int wr, int wc, int fr, int fq, int ui) const {
;         const int col0 = u.pn * BM + wc * 32 + 8 * fq;
;         const size_t off0 = ((size_t)(u.pm * (D / 64) + (col0 >> 6)) * 256 + wr * 64 + fr) * 64 + (col0 & 63);
;         f32x4 cr[2][2];
; #pragma unroll
;         for (int bj = 0; bj < 2; ++bj)
; #pragma unroll
;             for (int n = 0; n < 2; ++n) cr[bj][n] = *(const f32x4*)(cres + col0 + bj * HALF + n * 4);
;         u32x4 xb[3][2];
;     ...
;         EPIRES_LOAD(0, 0); EPIRES_LOAD(1, 1); EPIRES_LOAD(2, 2);
; #pragma unroll
;         for (int g = 0; g < 8; ++g) {
;             const int ai = g >> 2, m = g & 3;
;             const int row_ = u.pm * BM + ai * HALF + wr * 64 + m * 16 + fr;
;             float sq = 0.f;
; #pragma unroll
;             for (int bj = 0; bj < 2; ++bj) {
;                 u32x4 xs;
; #pragma unroll
;                 for (int n = 0; n < 2; ++n) {
;                     const unsigned p0 = xb[g % 3][bj][2 * n], p1 = xb[g % 3][bj][2 * n + 1];
;                     const f32x4 xo = {__builtin_bit_cast(float, p0 << 16), __builtin_bit_cast(float, p0 & 0xFFFF0000u), __builtin_bit_cast(float, p1 << 16), __builtin_bit_cast(float, p1 & 0xFFFF0000u)};
;                     const f32x4 xn = xo + cr[bj][n] * acc[ai][bj][m][n];
;                     sq += (xn[0] * xn[0] + xn[1] * xn[1]) + (xn[2] * xn[2] + xn[3] * xn[3]);
;                     if (n == 0) { xs.x = cvt_pk_bf16(xn[0], xn[1]); xs.y = cvt_pk_bf16(xn[2], xn[3]); } else { xs.z = cvt_pk_bf16(xn[0], xn[1]); xs.w = cvt_pk_bf16(xn[2], xn[3]); }
;                 }
;                 *(u32x4*)(x + EPIRES_OFF(g, bj)) = xs;
;             }
;             sq += __shfl_xor(sq, 16); sq += __shfl_xor(sq, 32);
;             if (fq == 0) ss[(size_t)row_ * 32 + u.pn * 4 + wc] = sq;
.LBB0_1399:
	s_lshl_b32 s18, s48, 8
	s_or_b32 s20, s18, s39
	s_lshl_b32 s18, s49, 5
	s_ashr_i32 s19, s20, 6
	s_add_i32 s18, s19, s18
	s_ashr_i32 s19, s18, 31
	v_or_b32_e32 v88, s20, v194
	v_bitop3_b32 v128, s20, 56, v194 bitop3:0xc8
	s_lshl_b64 s[18:19], s[18:19], 15
	v_ashrrev_i32_e32 v89, 31, v88
	v_lshl_add_u64 v[146:147], v[186:187], 0, s[18:19]
	v_lshlrev_b32_e32 v128, 1, v128
	v_lshl_add_u64 v[92:93], v[88:89], 2, s[10:11]
	v_lshl_add_u64 v[188:189], v[146:147], 0, v[128:129]
	global_load_dwordx4 v[100:103], v[92:93], off offset:16
	global_load_dwordx4 v[108:111], v[92:93], off
	global_load_dwordx4 v[88:91], v[92:93], off offset:528
	s_nop 0
	global_load_dwordx4 v[92:95], v[92:93], off offset:512
	s_mov_b32 s18, 0x10000
	global_load_dwordx4 v[166:169], v[188:189], off
	v_add_co_u32_e32 v192, vcc, s18, v188
	s_mov_b32 s18, 0x11000
	s_nop 0
	v_addc_co_u32_e32 v193, vcc, 0, v189, vcc
	v_add_co_u32_e32 v146, vcc, s18, v188
	v_xor_b32_e32 v128, 16, v228
	s_nop 0
	v_addc_co_u32_e32 v147, vcc, 0, v189, vcc
	global_load_dwordx4 v[162:165], v[146:147], off offset:-4096
	global_load_dwordx4 v[158:161], v[188:189], off offset:2048
	global_load_dwordx4 v[154:157], v[192:193], off offset:2048
	v_add_co_u32_e32 v148, vcc, s58, v188
	v_add_u32_e32 v172, 64, v171
	s_nop 0
	v_addc_co_u32_e32 v149, vcc, 0, v189, vcc
	global_load_dwordx4 v[150:153], v[148:149], off
	s_nop 0
	global_load_dwordx4 v[146:149], v[146:147], off
	v_cmp_lt_i32_e32 vcc, v128, v172
	v_xor_b32_e32 v173, 32, v228
	s_lshl_b32 s18, s48, 2
	v_cndmask_b32_e32 v128, v228, v128, vcc
	v_cmp_lt_i32_e32 vcc, v173, v172
	v_lshlrev_b32_e32 v128, 2, v128
	v_lshl_add_u32 v190, s49, 8, v184
	v_cndmask_b32_e32 v172, v228, v173, vcc
	v_lshlrev_b32_e32 v196, 2, v172
	s_ashr_i32 s19, s18, 31
	s_waitcnt vmcnt(0)
	v_lshlrev_b32_e32 v172, 16, v166
	v_and_b32_e32 v173, 0xffff0000, v166
	v_lshlrev_b32_e32 v166, 16, v167
	v_and_b32_e32 v167, 0xffff0000, v167
	v_pk_fma_f32 v[144:145], v[144:145], v[110:111], v[166:167]
	v_pk_fma_f32 v[142:143], v[142:143], v[108:109], v[172:173]
	v_mul_f32_e32 v167, v145, v145
	v_mul_f32_e32 v166, v143, v143
	v_fmac_f32_e32 v166, v142, v142
	v_fmac_f32_e32 v167, v144, v144
	v_add_f32_e32 v172, v166, v167
	v_cvt_pk_bf16_f32 v142, v142, v143
	v_cvt_pk_bf16_f32 v143, v144, v145
	v_lshlrev_b32_e32 v144, 16, v168
	v_and_b32_e32 v145, 0xffff0000, v168
	v_lshlrev_b32_e32 v166, 16, v169
	v_and_b32_e32 v167, 0xffff0000, v169
	v_pk_fma_f32 v[140:141], v[140:141], v[102:103], v[166:167]
	v_pk_fma_f32 v[138:139], v[138:139], v[100:101], v[144:145]
	v_mul_f32_e32 v145, v141, v141
	v_mul_f32_e32 v144, v139, v139
	v_fmac_f32_e32 v144, v138, v138
	v_fmac_f32_e32 v145, v140, v140
	v_add_f32_e32 v144, v144, v145
	v_add_f32_e32 v166, v172, v144
	v_cvt_pk_bf16_f32 v144, v138, v139
	v_cvt_pk_bf16_f32 v145, v140, v141
	v_lshlrev_b32_e32 v138, 16, v162
	v_and_b32_e32 v139, 0xffff0000, v162
	v_lshlrev_b32_e32 v140, 16, v163
	v_and_b32_e32 v141, 0xffff0000, v163
	v_pk_fma_f32 v[136:137], v[136:137], v[94:95], v[140:141]
	v_pk_fma_f32 v[134:135], v[134:135], v[92:93], v[138:139]
	v_mul_f32_e32 v139, v137, v137
	v_mul_f32_e32 v138, v135, v135
	v_fmac_f32_e32 v138, v134, v134
	v_fmac_f32_e32 v139, v136, v136
	v_add_f32_e32 v138, v138, v139
	v_add_f32_e32 v140, v166, v138
	v_cvt_pk_bf16_f32 v134, v134, v135
	v_cvt_pk_bf16_f32 v135, v136, v137
	v_lshlrev_b32_e32 v136, 16, v164
	v_and_b32_e32 v137, 0xffff0000, v164
	v_lshlrev_b32_e32 v138, 16, v165
	v_and_b32_e32 v139, 0xffff0000, v165
	v_pk_fma_f32 v[132:133], v[132:133], v[90:91], v[138:139]
	v_pk_fma_f32 v[130:131], v[130:131], v[88:89], v[136:137]
	v_mul_f32_e32 v137, v133, v133
	v_mul_f32_e32 v136, v131, v131
	v_fmac_f32_e32 v136, v130, v130
	v_fmac_f32_e32 v137, v132, v132
	v_add_f32_e32 v136, v136, v137
	v_add_f32_e32 v138, v136, v140
	v_cvt_pk_bf16_f32 v136, v130, v131
	ds_bpermute_b32 v130, v128, v138
	v_cvt_pk_bf16_f32 v137, v132, v133
	global_store_dwordx4 v[188:189], v[142:145], off sc1
	global_store_dwordx4 v[192:193], v[134:137], off sc1
	s_waitcnt lgkmcnt(0)
	v_add_f32_e32 v130, v138, v130
	ds_bpermute_b32 v131, v196, v130
	s_and_saveexec_b64 s[20:21], s[4:5]
	s_cbranch_execz .LBB0_1401
	v_ashrrev_i32_e32 v191, 31, v190
	v_lshlrev_b64 v[132:133], 7, v[190:191]
	v_lshl_add_u64 v[132:133], s[12:13], 0, v[132:133]
	v_lshl_add_u64 v[132:133], s[18:19], 2, v[132:133]
	s_lshl_b32 s64, s36, 2
	v_lshl_add_u64 v[132:133], v[132:133], 0, s[64:65]
	s_waitcnt lgkmcnt(0)
	v_add_f32_e32 v130, v130, v131
	global_store_dword v[132:133], v130, off sc1
; __device__ __forceinline__ unsigned cvt_pk_bf16(float lo, float hi) { const f32x2_t v = {lo, hi}; const bf16x2_t b = __builtin_convertvector(v, bf16x2_t); return __builtin_bit_cast(unsigned, b); }
; #define EPIRES_LOAD(buf, g) do { _Pragma("unroll") for (int bj = 0; bj < 2; ++bj) xb[buf][bj] = *(const u32x4*)(x + EPIRES_OFF(g, bj)); } while (0)
;     __device__ __forceinline__ void operator()(const f32x4 (&acc)[2][2][4][2], const Unit& u, int wr, int wc, int fr, int fq, int ui) const {
;     ...
;         for (int g = 0; g < 8; ++g) {
;             const int ai = g >> 2, m = g & 3;
;             const int row_ = u.pm * BM + ai * HALF + wr * 64 + m * 16 + fr;
;             float sq = 0.f;
; #pragma unroll
;             for (int bj = 0; bj < 2; ++bj) {
;                 u32x4 xs;
; #pragma unroll
;                 for (int n = 0; n < 2; ++n) {
;                     const unsigned p0 = xb[g % 3][bj][2 * n], p1 = xb[g % 3][bj][2 * n + 1];
;                     const f32x4 xo = {__builtin_bit_cast(float, p0 << 16), __builtin_bit_cast(float, p0 & 0xFFFF0000u), __builtin_bit_cast(float, p1 << 16), __builtin_bit_cast(float, p1 & 0xFFFF0000u)};
;                     const f32x4 xn = xo + cr[bj][n] * acc[ai][bj][m][n];
;                     sq += (xn[0] * xn[0] + xn[1] * xn[1]) + (xn[2] * xn[2] + xn[3] * xn[3]);
;                     if (n == 0) { xs.x = cvt_pk_bf16(xn[0], xn[1]); xs.y = cvt_pk_bf16(xn[2], xn[3]); } else { xs.z = cvt_pk_bf16(xn[0], xn[1]); xs.w = cvt_pk_bf16(xn[2], xn[3]); }
;                 }
;                 *(u32x4*)(x + EPIRES_OFF(g, bj)) = xs;
;             }
;             sq += __shfl_xor(sq, 16); sq += __shfl_xor(sq, 32);
;             if (fq == 0) ss[(size_t)row_ * 32 + u.pn * 4 + wc] = sq;
;             if (g + 3 < 8) EPIRES_LOAD(g % 3, g + 3);
.LBB0_1401:
	s_or_b64 exec, exec, s[20:21]
	v_add_co_u32_e32 v130, vcc, 0x1000, v188
	v_lshlrev_b32_e32 v140, 16, v158
	s_waitcnt lgkmcnt(0)
	v_addc_co_u32_e32 v131, vcc, 0, v189, vcc
	v_add_co_u32_e32 v132, vcc, 0x11000, v188
	v_and_b32_e32 v141, 0xffff0000, v158
	s_nop 0
	v_addc_co_u32_e32 v133, vcc, 0, v189, vcc
	global_load_dwordx4 v[134:137], v[130:131], off offset:2048
	s_nop 0
	global_load_dwordx4 v[130:133], v[132:133], off offset:2048
	v_lshlrev_b32_e32 v142, 16, v159
	v_and_b32_e32 v143, 0xffff0000, v159
	v_pk_fma_f32 v[126:127], v[126:127], v[110:111], v[142:143]
	v_pk_fma_f32 v[124:125], v[124:125], v[108:109], v[140:141]
	v_mul_f32_e32 v141, v127, v127
	v_mul_f32_e32 v140, v125, v125
	v_fmac_f32_e32 v140, v124, v124
	v_fmac_f32_e32 v141, v126, v126
	v_add_f32_e32 v142, v140, v141
	v_cvt_pk_bf16_f32 v124, v124, v125
	v_cvt_pk_bf16_f32 v125, v126, v127
	v_lshlrev_b32_e32 v126, 16, v160
	v_and_b32_e32 v127, 0xffff0000, v160
	v_lshlrev_b32_e32 v140, 16, v161
	v_and_b32_e32 v141, 0xffff0000, v161
	v_pk_fma_f32 v[122:123], v[122:123], v[102:103], v[140:141]
	v_pk_fma_f32 v[120:121], v[120:121], v[100:101], v[126:127]
	v_mul_f32_e32 v127, v123, v123
	v_mul_f32_e32 v126, v121, v121
	v_fmac_f32_e32 v126, v120, v120
	v_fmac_f32_e32 v127, v122, v122
	v_add_f32_e32 v126, v126, v127
	v_add_f32_e32 v142, v142, v126
	v_lshlrev_b32_e32 v126, 16, v154
	v_and_b32_e32 v127, 0xffff0000, v154
	v_lshlrev_b32_e32 v140, 16, v155
	v_and_b32_e32 v141, 0xffff0000, v155
	v_pk_fma_f32 v[118:119], v[118:119], v[94:95], v[140:141]
	v_pk_fma_f32 v[116:117], v[116:117], v[92:93], v[126:127]
	v_mul_f32_e32 v127, v119, v119
	v_mul_f32_e32 v126, v117, v117
	v_fmac_f32_e32 v126, v116, v116
	v_fmac_f32_e32 v127, v118, v118
	v_add_f32_e32 v126, v126, v127
	v_add_f32_e32 v144, v142, v126
	v_lshlrev_b32_e32 v126, 16, v156
	v_and_b32_e32 v127, 0xffff0000, v156
	v_lshlrev_b32_e32 v140, 16, v157
	v_and_b32_e32 v141, 0xffff0000, v157
	v_pk_fma_f32 v[140:141], v[114:115], v[90:91], v[140:141]
	v_pk_fma_f32 v[142:143], v[112:113], v[88:89], v[126:127]
	v_mul_f32_e32 v113, v141, v141
	v_mul_f32_e32 v112, v143, v143
	v_fmac_f32_e32 v112, v142, v142
	v_fmac_f32_e32 v113, v140, v140
	v_add_f32_e32 v112, v112, v113
	v_add_f32_e32 v112, v112, v144
	ds_bpermute_b32 v113, v128, v112
	s_mov_b64 s[20:21], 0x10800
	v_lshl_add_u64 v[138:139], v[188:189], 0, s[20:21]
	v_cvt_pk_bf16_f32 v126, v120, v121
	v_cvt_pk_bf16_f32 v127, v122, v123
	s_waitcnt lgkmcnt(0)
	v_add_f32_e32 v112, v112, v113
	ds_bpermute_b32 v113, v196, v112
	v_cvt_pk_bf16_f32 v114, v116, v117
	v_cvt_pk_bf16_f32 v115, v118, v119
	v_cvt_pk_bf16_f32 v116, v142, v143
	v_cvt_pk_bf16_f32 v117, v140, v141
	global_store_dwordx4 v[188:189], v[124:127], off offset:2048 sc1
	global_store_dwordx4 v[138:139], v[114:117], off sc1
	s_and_saveexec_b64 s[20:21], s[4:5]
	s_cbranch_execz .LBB0_1403
	v_or_b32_e32 v114, 16, v190
	v_ashrrev_i32_e32 v115, 31, v114
	s_waitcnt lgkmcnt(0)
	v_add_f32_e32 v116, v112, v113
	v_lshlrev_b64 v[112:113], 7, v[114:115]
	v_lshl_add_u64 v[112:113], s[12:13], 0, v[112:113]
	v_lshl_add_u64 v[112:113], s[18:19], 2, v[112:113]
	s_lshl_b32 s64, s36, 2
	v_lshl_add_u64 v[112:113], v[112:113], 0, s[64:65]
	global_store_dword v[112:113], v116, off sc1
.LBB0_1403:
	s_or_b64 exec, exec, s[20:21]
	v_add_co_u32_e32 v112, vcc, 0x4000, v188
	v_lshlrev_b32_e32 v124, 16, v150
	s_waitcnt lgkmcnt(0)
	v_addc_co_u32_e32 v113, vcc, 0, v189, vcc
	v_add_co_u32_e32 v114, vcc, 0x14000, v188
	v_and_b32_e32 v125, 0xffff0000, v150
	s_nop 0
	v_addc_co_u32_e32 v115, vcc, 0, v189, vcc
	global_load_dwordx4 v[116:119], v[112:113], off
	s_nop 0
	global_load_dwordx4 v[112:115], v[114:115], off
	v_lshlrev_b32_e32 v126, 16, v151
	v_and_b32_e32 v127, 0xffff0000, v151
	v_pk_fma_f32 v[106:107], v[106:107], v[110:111], v[126:127]
	v_pk_fma_f32 v[104:105], v[104:105], v[108:109], v[124:125]
	v_mul_f32_e32 v125, v107, v107
	v_mul_f32_e32 v124, v105, v105
	v_fmac_f32_e32 v124, v104, v104
	v_fmac_f32_e32 v125, v106, v106
	v_add_f32_e32 v126, v124, v125
	v_cvt_pk_bf16_f32 v104, v104, v105
	v_cvt_pk_bf16_f32 v105, v106, v107
	v_lshlrev_b32_e32 v106, 16, v152
	v_and_b32_e32 v107, 0xffff0000, v152
	v_lshlrev_b32_e32 v124, 16, v153
	v_and_b32_e32 v125, 0xffff0000, v153
	v_pk_fma_f32 v[98:99], v[98:99], v[102:103], v[124:125]
	v_pk_fma_f32 v[96:97], v[96:97], v[100:101], v[106:107]
	v_mul_f32_e32 v107, v99, v99
	v_mul_f32_e32 v106, v97, v97
	v_fmac_f32_e32 v106, v96, v96
	v_fmac_f32_e32 v107, v98, v98
	v_add_f32_e32 v106, v106, v107
	v_add_f32_e32 v126, v126, v106
	v_lshlrev_b32_e32 v106, 16, v146
	v_and_b32_e32 v107, 0xffff0000, v146
	v_lshlrev_b32_e32 v124, 16, v147
	v_and_b32_e32 v125, 0xffff0000, v147
	v_pk_fma_f32 v[86:87], v[86:87], v[94:95], v[124:125]
	v_pk_fma_f32 v[84:85], v[84:85], v[92:93], v[106:107]
	v_mul_f32_e32 v107, v87, v87
	v_mul_f32_e32 v106, v85, v85
	v_fmac_f32_e32 v106, v84, v84
	v_fmac_f32_e32 v107, v86, v86
	v_add_f32_e32 v106, v106, v107
	v_add_f32_e32 v138, v126, v106
	v_lshlrev_b32_e32 v106, 16, v148
	v_and_b32_e32 v107, 0xffff0000, v148
	v_lshlrev_b32_e32 v124, 16, v149
	v_and_b32_e32 v125, 0xffff0000, v149
	v_pk_fma_f32 v[124:125], v[82:83], v[90:91], v[124:125]
	v_pk_fma_f32 v[126:127], v[80:81], v[88:89], v[106:107]
	v_mul_f32_e32 v81, v125, v125
	v_mul_f32_e32 v80, v127, v127
	v_fmac_f32_e32 v80, v126, v126
	v_fmac_f32_e32 v81, v124, v124
	v_add_f32_e32 v80, v80, v81
	v_add_f32_e32 v80, v80, v138
	ds_bpermute_b32 v81, v128, v80
	s_mov_b64 s[20:21], 0x1000
	v_lshl_add_u64 v[120:121], v[188:189], 0, s[20:21]
	s_mov_b64 s[20:21], 0x11000
	v_lshl_add_u64 v[122:123], v[188:189], 0, s[20:21]
	s_waitcnt lgkmcnt(0)
	v_add_f32_e32 v80, v80, v81
	ds_bpermute_b32 v81, v196, v80
	v_cvt_pk_bf16_f32 v106, v96, v97
	v_cvt_pk_bf16_f32 v107, v98, v99
	v_cvt_pk_bf16_f32 v82, v84, v85
	v_cvt_pk_bf16_f32 v83, v86, v87
	v_cvt_pk_bf16_f32 v84, v126, v127
	v_cvt_pk_bf16_f32 v85, v124, v125
	global_store_dwordx4 v[120:121], v[104:107], off sc1
	global_store_dwordx4 v[122:123], v[82:85], off sc1
	s_and_saveexec_b64 s[20:21], s[4:5]
	s_cbranch_execz .LBB0_1405
	v_or_b32_e32 v82, 32, v190
	v_ashrrev_i32_e32 v83, 31, v82
	s_waitcnt lgkmcnt(0)
	v_add_f32_e32 v84, v80, v81
	v_lshlrev_b64 v[80:81], 7, v[82:83]
	v_lshl_add_u64 v[80:81], s[12:13], 0, v[80:81]
	v_lshl_add_u64 v[80:81], s[18:19], 2, v[80:81]
	s_lshl_b32 s64, s36, 2
	v_lshl_add_u64 v[80:81], v[80:81], 0, s[64:65]
	global_store_dword v[80:81], v84, off sc1
; __device__ __forceinline__ unsigned cvt_pk_bf16(float lo, float hi) { const f32x2_t v = {lo, hi}; const bf16x2_t b = __builtin_convertvector(v, bf16x2_t); return __builtin_bit_cast(unsigned, b); }
; #define EPIRES_LOAD(buf, g) do { _Pragma("unroll") for (int bj = 0; bj < 2; ++bj) xb[buf][bj] = *(const u32x4*)(x + EPIRES_OFF(g, bj)); } while (0)
;     __device__ __forceinline__ void operator()(const f32x4 (&acc)[2][2][4][2], const Unit& u, int wr, int wc, int fr, int fq, int ui) const {
;     ...
;         for (int g = 0; g < 8; ++g) {
;             const int ai = g >> 2, m = g & 3;
;             const int row_ = u.pm * BM + ai * HALF + wr * 64 + m * 16 + fr;
;             float sq = 0.f;
; #pragma unroll
;             for (int bj = 0; bj < 2; ++bj) {
;                 u32x4 xs;
; #pragma unroll
;                 for (int n = 0; n < 2; ++n) {
;                     const unsigned p0 = xb[g % 3][bj][2 * n], p1 = xb[g % 3][bj][2 * n + 1];
;                     const f32x4 xo = {__builtin_bit_cast(float, p0 << 16), __builtin_bit_cast(float, p0 & 0xFFFF0000u), __builtin_bit_cast(float, p1 << 16), __builtin_bit_cast(float, p1 & 0xFFFF0000u)};
;                     const f32x4 xn = xo + cr[bj][n] * acc[ai][bj][m][n];
;                     sq += (xn[0] * xn[0] + xn[1] * xn[1]) + (xn[2] * xn[2] + xn[3] * xn[3]);
;                     if (n == 0) { xs.x = cvt_pk_bf16(xn[0], xn[1]); xs.y = cvt_pk_bf16(xn[2], xn[3]); } else { xs.z = cvt_pk_bf16(xn[0], xn[1]); xs.w = cvt_pk_bf16(xn[2], xn[3]); }
;                 }
;                 *(u32x4*)(x + EPIRES_OFF(g, bj)) = xs;
;             }
;             sq += __shfl_xor(sq, 16); sq += __shfl_xor(sq, 32);
;             if (fq == 0) ss[(size_t)row_ * 32 + u.pn * 4 + wc] = sq;
;             if (g + 3 < 8) EPIRES_LOAD(g % 3, g + 3);
.LBB0_1405:
	s_or_b64 exec, exec, s[20:21]
	v_add_co_u32_e32 v80, vcc, 0x4000, v188
	s_waitcnt vmcnt(7)
	v_lshlrev_b32_e32 v104, 16, v134
	s_waitcnt lgkmcnt(0)
	v_addc_co_u32_e32 v81, vcc, 0, v189, vcc
	v_add_co_u32_e32 v82, vcc, 0x14000, v188
	v_and_b32_e32 v105, 0xffff0000, v134
	s_nop 0
	v_addc_co_u32_e32 v83, vcc, 0, v189, vcc
	global_load_dwordx4 v[84:87], v[80:81], off offset:2048
	s_nop 0
	global_load_dwordx4 v[80:83], v[82:83], off offset:2048
	v_lshlrev_b32_e32 v106, 16, v135
	v_and_b32_e32 v107, 0xffff0000, v135
	v_pk_fma_f32 v[78:79], v[78:79], v[110:111], v[106:107]
	v_pk_fma_f32 v[76:77], v[76:77], v[108:109], v[104:105]
	v_mul_f32_e32 v105, v79, v79
	v_mul_f32_e32 v104, v77, v77
	v_fmac_f32_e32 v104, v76, v76
	v_fmac_f32_e32 v105, v78, v78
	v_add_f32_e32 v106, v104, v105
	v_cvt_pk_bf16_f32 v76, v76, v77
	v_cvt_pk_bf16_f32 v77, v78, v79
	v_lshlrev_b32_e32 v78, 16, v136
	v_and_b32_e32 v79, 0xffff0000, v136
	v_lshlrev_b32_e32 v104, 16, v137
	v_and_b32_e32 v105, 0xffff0000, v137
	v_pk_fma_f32 v[74:75], v[74:75], v[102:103], v[104:105]
	v_pk_fma_f32 v[72:73], v[72:73], v[100:101], v[78:79]
	v_mul_f32_e32 v79, v75, v75
	v_mul_f32_e32 v78, v73, v73
	v_fmac_f32_e32 v78, v72, v72
	v_fmac_f32_e32 v79, v74, v74
	v_add_f32_e32 v78, v78, v79
	v_add_f32_e32 v106, v106, v78
	s_waitcnt vmcnt(8)
	v_lshlrev_b32_e32 v78, 16, v130
	v_and_b32_e32 v79, 0xffff0000, v130
	v_lshlrev_b32_e32 v104, 16, v131
	v_and_b32_e32 v105, 0xffff0000, v131
	v_pk_fma_f32 v[70:71], v[70:71], v[94:95], v[104:105]
	v_pk_fma_f32 v[68:69], v[68:69], v[92:93], v[78:79]
	v_mul_f32_e32 v79, v71, v71
	v_mul_f32_e32 v78, v69, v69
	v_fmac_f32_e32 v78, v68, v68
	v_fmac_f32_e32 v79, v70, v70
	v_add_f32_e32 v78, v78, v79
	v_add_f32_e32 v120, v106, v78
	v_lshlrev_b32_e32 v78, 16, v132
	v_and_b32_e32 v79, 0xffff0000, v132
	v_lshlrev_b32_e32 v104, 16, v133
	v_and_b32_e32 v105, 0xffff0000, v133
	v_pk_fma_f32 v[104:105], v[66:67], v[90:91], v[104:105]
	v_pk_fma_f32 v[106:107], v[64:65], v[88:89], v[78:79]
	v_mul_f32_e32 v65, v105, v105
	v_mul_f32_e32 v64, v107, v107
	v_fmac_f32_e32 v64, v106, v106
	v_fmac_f32_e32 v65, v104, v104
	v_add_f32_e32 v64, v64, v65
	v_add_f32_e32 v64, v64, v120
	ds_bpermute_b32 v65, v128, v64
	s_mov_b64 s[20:21], 0x1800
	v_lshl_add_u64 v[96:97], v[188:189], 0, s[20:21]
	s_mov_b64 s[20:21], 0x11800
	v_lshl_add_u64 v[98:99], v[188:189], 0, s[20:21]
	s_waitcnt lgkmcnt(0)
	v_add_f32_e32 v64, v64, v65
	ds_bpermute_b32 v65, v196, v64
	v_cvt_pk_bf16_f32 v78, v72, v73
	v_cvt_pk_bf16_f32 v79, v74, v75
	v_cvt_pk_bf16_f32 v66, v68, v69
	v_cvt_pk_bf16_f32 v67, v70, v71
	v_cvt_pk_bf16_f32 v68, v106, v107
	v_cvt_pk_bf16_f32 v69, v104, v105
	global_store_dwordx4 v[96:97], v[76:79], off sc1
	global_store_dwordx4 v[98:99], v[66:69], off sc1
	s_and_saveexec_b64 s[20:21], s[4:5]
	s_cbranch_execz .LBB0_1407
	v_or_b32_e32 v66, 48, v190
	v_ashrrev_i32_e32 v67, 31, v66
	s_waitcnt lgkmcnt(0)
	v_add_f32_e32 v68, v64, v65
	v_lshlrev_b64 v[64:65], 7, v[66:67]
	v_lshl_add_u64 v[64:65], s[12:13], 0, v[64:65]
	v_lshl_add_u64 v[64:65], s[18:19], 2, v[64:65]
	s_lshl_b32 s64, s36, 2
	v_lshl_add_u64 v[64:65], v[64:65], 0, s[64:65]
	global_store_dword v[64:65], v68, off sc1
.LBB0_1407:
	s_or_b64 exec, exec, s[20:21]
	v_add_co_u32_e32 v64, vcc, 0x5000, v188
	s_waitcnt vmcnt(7)
	v_lshlrev_b32_e32 v78, 16, v116
	s_waitcnt lgkmcnt(0)
	v_addc_co_u32_e32 v65, vcc, 0, v189, vcc
	v_add_co_u32_e32 v66, vcc, 0x15000, v188
	v_and_b32_e32 v79, 0xffff0000, v116
	s_nop 0
	v_addc_co_u32_e32 v67, vcc, 0, v189, vcc
	global_load_dwordx4 v[68:71], v[64:65], off
	s_nop 0
	global_load_dwordx4 v[64:67], v[66:67], off
	v_lshlrev_b32_e32 v96, 16, v117
	v_and_b32_e32 v97, 0xffff0000, v117
	v_pk_fma_f32 v[62:63], v[62:63], v[110:111], v[96:97]
	v_pk_fma_f32 v[60:61], v[60:61], v[108:109], v[78:79]
	v_mul_f32_e32 v78, v63, v63
	v_mul_f32_e32 v73, v61, v61
	v_fmac_f32_e32 v73, v60, v60
	v_fmac_f32_e32 v78, v62, v62
	v_add_f32_e32 v73, v73, v78
	v_cvt_pk_bf16_f32 v60, v60, v61
	v_cvt_pk_bf16_f32 v61, v62, v63
	v_lshlrev_b32_e32 v62, 16, v118
	v_and_b32_e32 v63, 0xffff0000, v118
	v_lshlrev_b32_e32 v78, 16, v119
	v_and_b32_e32 v79, 0xffff0000, v119
	v_pk_fma_f32 v[58:59], v[58:59], v[102:103], v[78:79]
	v_pk_fma_f32 v[56:57], v[56:57], v[100:101], v[62:63]
	v_mul_f32_e32 v63, v59, v59
	v_mul_f32_e32 v62, v57, v57
	v_fmac_f32_e32 v62, v56, v56
	v_fmac_f32_e32 v63, v58, v58
	v_add_f32_e32 v62, v62, v63
	v_add_f32_e32 v73, v73, v62
	s_waitcnt vmcnt(8)
	v_lshlrev_b32_e32 v62, 16, v112
	v_and_b32_e32 v63, 0xffff0000, v112
	v_lshlrev_b32_e32 v78, 16, v113
	v_and_b32_e32 v79, 0xffff0000, v113
	v_pk_fma_f32 v[54:55], v[54:55], v[94:95], v[78:79]
	v_pk_fma_f32 v[52:53], v[52:53], v[92:93], v[62:63]
	v_mul_f32_e32 v63, v55, v55
	v_mul_f32_e32 v62, v53, v53
	v_fmac_f32_e32 v62, v52, v52
	v_fmac_f32_e32 v63, v54, v54
	v_add_f32_e32 v62, v62, v63
	v_add_f32_e32 v73, v73, v62
	v_lshlrev_b32_e32 v62, 16, v114
	v_and_b32_e32 v63, 0xffff0000, v114
	v_lshlrev_b32_e32 v78, 16, v115
	v_and_b32_e32 v79, 0xffff0000, v115
	v_pk_fma_f32 v[78:79], v[50:51], v[90:91], v[78:79]
	v_pk_fma_f32 v[96:97], v[48:49], v[88:89], v[62:63]
	v_mul_f32_e32 v49, v79, v79
	v_mul_f32_e32 v48, v97, v97
	v_fmac_f32_e32 v48, v96, v96
	v_fmac_f32_e32 v49, v78, v78
	v_add_f32_e32 v48, v48, v49
	v_add_f32_e32 v48, v48, v73
	ds_bpermute_b32 v49, v128, v48
	s_mov_b64 s[20:21], 0x4000
	v_lshl_add_u64 v[74:75], v[188:189], 0, s[20:21]
	s_mov_b64 s[20:21], 0x14000
	v_lshl_add_u64 v[76:77], v[188:189], 0, s[20:21]
	s_waitcnt lgkmcnt(0)
	v_add_f32_e32 v48, v48, v49
	ds_bpermute_b32 v49, v196, v48
	v_add_u32_e32 v72, 0x80, v190
	v_cvt_pk_bf16_f32 v62, v56, v57
	v_cvt_pk_bf16_f32 v63, v58, v59
	v_cvt_pk_bf16_f32 v50, v52, v53
	v_cvt_pk_bf16_f32 v51, v54, v55
	v_cvt_pk_bf16_f32 v52, v96, v97
	v_cvt_pk_bf16_f32 v53, v78, v79
	global_store_dwordx4 v[74:75], v[60:63], off sc1
	global_store_dwordx4 v[76:77], v[50:53], off sc1
	s_and_saveexec_b64 s[20:21], s[4:5]
	s_cbranch_execz .LBB0_1409
	v_ashrrev_i32_e32 v73, 31, v72
	v_lshlrev_b64 v[50:51], 7, v[72:73]
	v_lshl_add_u64 v[50:51], s[12:13], 0, v[50:51]
	v_lshl_add_u64 v[50:51], s[18:19], 2, v[50:51]
	s_lshl_b32 s64, s36, 2
	v_lshl_add_u64 v[50:51], v[50:51], 0, s[64:65]
	s_waitcnt lgkmcnt(0)
	v_add_f32_e32 v48, v48, v49
	global_store_dword v[50:51], v48, off sc1
; __device__ __forceinline__ unsigned cvt_pk_bf16(float lo, float hi) { const f32x2_t v = {lo, hi}; const bf16x2_t b = __builtin_convertvector(v, bf16x2_t); return __builtin_bit_cast(unsigned, b); }
; #define EPIRES_LOAD(buf, g) do { _Pragma("unroll") for (int bj = 0; bj < 2; ++bj) xb[buf][bj] = *(const u32x4*)(x + EPIRES_OFF(g, bj)); } while (0)
;     __device__ __forceinline__ void operator()(const f32x4 (&acc)[2][2][4][2], const Unit& u, int wr, int wc, int fr, int fq, int ui) const {
;     ...
;         for (int g = 0; g < 8; ++g) {
;             const int ai = g >> 2, m = g & 3;
;             const int row_ = u.pm * BM + ai * HALF + wr * 64 + m * 16 + fr;
;             float sq = 0.f;
; #pragma unroll
;             for (int bj = 0; bj < 2; ++bj) {
;                 u32x4 xs;
; #pragma unroll
;                 for (int n = 0; n < 2; ++n) {
;                     const unsigned p0 = xb[g % 3][bj][2 * n], p1 = xb[g % 3][bj][2 * n + 1];
;                     const f32x4 xo = {__builtin_bit_cast(float, p0 << 16), __builtin_bit_cast(float, p0 & 0xFFFF0000u), __builtin_bit_cast(float, p1 << 16), __builtin_bit_cast(float, p1 & 0xFFFF0000u)};
;                     const f32x4 xn = xo + cr[bj][n] * acc[ai][bj][m][n];
;                     sq += (xn[0] * xn[0] + xn[1] * xn[1]) + (xn[2] * xn[2] + xn[3] * xn[3]);
;                     if (n == 0) { xs.x = cvt_pk_bf16(xn[0], xn[1]); xs.y = cvt_pk_bf16(xn[2], xn[3]); } else { xs.z = cvt_pk_bf16(xn[0], xn[1]); xs.w = cvt_pk_bf16(xn[2], xn[3]); }
;                 }
;                 *(u32x4*)(x + EPIRES_OFF(g, bj)) = xs;
;             }
;             sq += __shfl_xor(sq, 16); sq += __shfl_xor(sq, 32);
;             if (fq == 0) ss[(size_t)row_ * 32 + u.pn * 4 + wc] = sq;
;             if (g + 3 < 8) EPIRES_LOAD(g % 3, g + 3);
.LBB0_1409:
	s_or_b64 exec, exec, s[20:21]
	v_add_co_u32_e32 v48, vcc, 0x5000, v188
	s_waitcnt vmcnt(7)
	v_lshlrev_b32_e32 v60, 16, v84
	s_waitcnt lgkmcnt(0)
	v_addc_co_u32_e32 v49, vcc, 0, v189, vcc
	v_add_co_u32_e32 v50, vcc, 0x15000, v188
	v_and_b32_e32 v61, 0xffff0000, v84
	s_nop 0
	v_addc_co_u32_e32 v51, vcc, 0, v189, vcc
	global_load_dwordx4 v[52:55], v[48:49], off offset:2048
	s_nop 0
	global_load_dwordx4 v[48:51], v[50:51], off offset:2048
	v_lshlrev_b32_e32 v62, 16, v85
	v_and_b32_e32 v63, 0xffff0000, v85
	v_pk_fma_f32 v[46:47], v[46:47], v[110:111], v[62:63]
	v_pk_fma_f32 v[44:45], v[44:45], v[108:109], v[60:61]
	v_mul_f32_e32 v61, v47, v47
	v_mul_f32_e32 v60, v45, v45
	v_fmac_f32_e32 v60, v44, v44
	v_fmac_f32_e32 v61, v46, v46
	v_add_f32_e32 v62, v60, v61
	v_cvt_pk_bf16_f32 v44, v44, v45
	v_cvt_pk_bf16_f32 v45, v46, v47
	v_lshlrev_b32_e32 v46, 16, v86
	v_and_b32_e32 v47, 0xffff0000, v86
	v_lshlrev_b32_e32 v60, 16, v87
	v_and_b32_e32 v61, 0xffff0000, v87
	v_pk_fma_f32 v[42:43], v[42:43], v[102:103], v[60:61]
	v_pk_fma_f32 v[40:41], v[40:41], v[100:101], v[46:47]
	v_mul_f32_e32 v47, v43, v43
	v_mul_f32_e32 v46, v41, v41
	v_fmac_f32_e32 v46, v40, v40
	v_fmac_f32_e32 v47, v42, v42
	v_add_f32_e32 v46, v46, v47
	v_add_f32_e32 v62, v62, v46
	s_waitcnt vmcnt(8)
	v_lshlrev_b32_e32 v46, 16, v80
	v_and_b32_e32 v47, 0xffff0000, v80
	v_lshlrev_b32_e32 v60, 16, v81
	v_and_b32_e32 v61, 0xffff0000, v81
	v_pk_fma_f32 v[38:39], v[38:39], v[94:95], v[60:61]
	v_pk_fma_f32 v[36:37], v[36:37], v[92:93], v[46:47]
	v_mul_f32_e32 v47, v39, v39
	v_mul_f32_e32 v46, v37, v37
	v_fmac_f32_e32 v46, v36, v36
	v_fmac_f32_e32 v47, v38, v38
	v_add_f32_e32 v46, v46, v47
	v_add_f32_e32 v73, v62, v46
	v_lshlrev_b32_e32 v46, 16, v82
	v_and_b32_e32 v47, 0xffff0000, v82
	v_lshlrev_b32_e32 v60, 16, v83
	v_and_b32_e32 v61, 0xffff0000, v83
	v_pk_fma_f32 v[60:61], v[34:35], v[90:91], v[60:61]
	v_pk_fma_f32 v[62:63], v[32:33], v[88:89], v[46:47]
	v_mul_f32_e32 v33, v61, v61
	v_mul_f32_e32 v32, v63, v63
	v_fmac_f32_e32 v32, v62, v62
	v_fmac_f32_e32 v33, v60, v60
	v_add_f32_e32 v32, v32, v33
	v_add_f32_e32 v32, v32, v73
	ds_bpermute_b32 v33, v128, v32
	s_mov_b64 s[20:21], 0x4800
	v_lshl_add_u64 v[56:57], v[188:189], 0, s[20:21]
	s_mov_b64 s[20:21], 0x14800
	v_lshl_add_u64 v[58:59], v[188:189], 0, s[20:21]
	s_waitcnt lgkmcnt(0)
	v_add_f32_e32 v32, v32, v33
	ds_bpermute_b32 v33, v196, v32
	v_cvt_pk_bf16_f32 v46, v40, v41
	v_cvt_pk_bf16_f32 v47, v42, v43
	v_cvt_pk_bf16_f32 v34, v36, v37
	v_cvt_pk_bf16_f32 v35, v38, v39
	v_cvt_pk_bf16_f32 v36, v62, v63
	v_cvt_pk_bf16_f32 v37, v60, v61
	global_store_dwordx4 v[56:57], v[44:47], off sc1
	global_store_dwordx4 v[58:59], v[34:37], off sc1
	s_and_saveexec_b64 s[20:21], s[4:5]
	s_cbranch_execz .LBB0_1411
	v_or_b32_e32 v34, 16, v72
	v_ashrrev_i32_e32 v35, 31, v34
	s_waitcnt lgkmcnt(0)
	v_add_f32_e32 v36, v32, v33
	v_lshlrev_b64 v[32:33], 7, v[34:35]
	v_lshl_add_u64 v[32:33], s[12:13], 0, v[32:33]
	v_lshl_add_u64 v[32:33], s[18:19], 2, v[32:33]
	s_lshl_b32 s64, s36, 2
	v_lshl_add_u64 v[32:33], v[32:33], 0, s[64:65]
	global_store_dword v[32:33], v36, off sc1
; __device__ __forceinline__ unsigned cvt_pk_bf16(float lo, float hi) { const f32x2_t v = {lo, hi}; const bf16x2_t b = __builtin_convertvector(v, bf16x2_t); return __builtin_bit_cast(unsigned, b); }
;     __device__ __forceinline__ void operator()(const f32x4 (&acc)[2][2][4][2], const Unit& u, int wr, int wc, int fr, int fq, int ui) const {
;     ...
;         for (int g = 0; g < 8; ++g) {
;             const int ai = g >> 2, m = g & 3;
;             const int row_ = u.pm * BM + ai * HALF + wr * 64 + m * 16 + fr;
;             float sq = 0.f;
; #pragma unroll
;             for (int bj = 0; bj < 2; ++bj) {
;                 u32x4 xs;
; #pragma unroll
;                 for (int n = 0; n < 2; ++n) {
;                     const unsigned p0 = xb[g % 3][bj][2 * n], p1 = xb[g % 3][bj][2 * n + 1];
;                     const f32x4 xo = {__builtin_bit_cast(float, p0 << 16), __builtin_bit_cast(float, p0 & 0xFFFF0000u), __builtin_bit_cast(float, p1 << 16), __builtin_bit_cast(float, p1 & 0xFFFF0000u)};
;                     const f32x4 xn = xo + cr[bj][n] * acc[ai][bj][m][n];
;                     sq += (xn[0] * xn[0] + xn[1] * xn[1]) + (xn[2] * xn[2] + xn[3] * xn[3]);
;                     if (n == 0) { xs.x = cvt_pk_bf16(xn[0], xn[1]); xs.y = cvt_pk_bf16(xn[2], xn[3]); } else { xs.z = cvt_pk_bf16(xn[0], xn[1]); xs.w = cvt_pk_bf16(xn[2], xn[3]); }
;                 }
;                 *(u32x4*)(x + EPIRES_OFF(g, bj)) = xs;
;             }
;             sq += __shfl_xor(sq, 16); sq += __shfl_xor(sq, 32);
;             if (fq == 0) ss[(size_t)row_ * 32 + u.pn * 4 + wc] = sq;
.LBB0_1411:
	s_or_b64 exec, exec, s[20:21]
	s_waitcnt vmcnt(7)
	v_lshlrev_b32_e32 v36, 16, v68
	v_and_b32_e32 v37, 0xffff0000, v68
	v_lshlrev_b32_e32 v38, 16, v69
	v_and_b32_e32 v39, 0xffff0000, v69
	v_pk_fma_f32 v[30:31], v[30:31], v[110:111], v[38:39]
	v_pk_fma_f32 v[28:29], v[28:29], v[108:109], v[36:37]
	v_mul_f32_e32 v37, v31, v31
	v_mul_f32_e32 v36, v29, v29
	v_fmac_f32_e32 v36, v28, v28
	v_fmac_f32_e32 v37, v30, v30
	v_add_f32_e32 v38, v36, v37
	v_cvt_pk_bf16_f32 v28, v28, v29
	v_cvt_pk_bf16_f32 v29, v30, v31
	v_lshlrev_b32_e32 v30, 16, v70
	v_and_b32_e32 v31, 0xffff0000, v70
	v_lshlrev_b32_e32 v36, 16, v71
	v_and_b32_e32 v37, 0xffff0000, v71
	v_pk_fma_f32 v[26:27], v[26:27], v[102:103], v[36:37]
	v_pk_fma_f32 v[24:25], v[24:25], v[100:101], v[30:31]
	v_mul_f32_e32 v31, v27, v27
	v_mul_f32_e32 v30, v25, v25
	v_fmac_f32_e32 v30, v24, v24
	v_fmac_f32_e32 v31, v26, v26
	v_add_f32_e32 v30, v30, v31
	v_add_f32_e32 v38, v38, v30
	s_waitcnt vmcnt(6)
	v_lshlrev_b32_e32 v30, 16, v64
	v_and_b32_e32 v31, 0xffff0000, v64
	v_lshlrev_b32_e32 v36, 16, v65
	v_and_b32_e32 v37, 0xffff0000, v65
	v_pk_fma_f32 v[22:23], v[22:23], v[94:95], v[36:37]
	v_pk_fma_f32 v[20:21], v[20:21], v[92:93], v[30:31]
	v_mul_f32_e32 v31, v23, v23
	v_mul_f32_e32 v30, v21, v21
	v_fmac_f32_e32 v30, v20, v20
	v_fmac_f32_e32 v31, v22, v22
	v_add_f32_e32 v30, v30, v31
	v_add_f32_e32 v40, v38, v30
	v_lshlrev_b32_e32 v30, 16, v66
	v_and_b32_e32 v31, 0xffff0000, v66
	v_lshlrev_b32_e32 v36, 16, v67
	v_and_b32_e32 v37, 0xffff0000, v67
	v_pk_fma_f32 v[36:37], v[18:19], v[90:91], v[36:37]
	v_pk_fma_f32 v[38:39], v[16:17], v[88:89], v[30:31]
	v_mul_f32_e32 v17, v37, v37
	v_mul_f32_e32 v16, v39, v39
	v_fmac_f32_e32 v16, v38, v38
	v_fmac_f32_e32 v17, v36, v36
	v_add_f32_e32 v16, v16, v17
	v_add_f32_e32 v16, v16, v40
	ds_bpermute_b32 v17, v128, v16
	s_mov_b64 s[20:21], 0x5000
	s_waitcnt lgkmcnt(1)
	v_lshl_add_u64 v[32:33], v[188:189], 0, s[20:21]
	s_mov_b64 s[20:21], 0x15000
	v_lshl_add_u64 v[34:35], v[188:189], 0, s[20:21]
	s_waitcnt lgkmcnt(0)
	v_add_f32_e32 v16, v16, v17
	ds_bpermute_b32 v17, v196, v16
	v_cvt_pk_bf16_f32 v30, v24, v25
	v_cvt_pk_bf16_f32 v31, v26, v27
	v_cvt_pk_bf16_f32 v18, v20, v21
	v_cvt_pk_bf16_f32 v19, v22, v23
	v_cvt_pk_bf16_f32 v20, v38, v39
	v_cvt_pk_bf16_f32 v21, v36, v37
	global_store_dwordx4 v[32:33], v[28:31], off sc1
	global_store_dwordx4 v[34:35], v[18:21], off sc1
	s_and_saveexec_b64 s[20:21], s[4:5]
	s_cbranch_execz .LBB0_1413
	v_or_b32_e32 v18, 32, v72
	v_ashrrev_i32_e32 v19, 31, v18
	s_waitcnt lgkmcnt(0)
	v_add_f32_e32 v20, v16, v17
	v_lshlrev_b64 v[16:17], 7, v[18:19]
	v_lshl_add_u64 v[16:17], s[12:13], 0, v[16:17]
	v_lshl_add_u64 v[16:17], s[18:19], 2, v[16:17]
	s_lshl_b32 s64, s36, 2
	v_lshl_add_u64 v[16:17], v[16:17], 0, s[64:65]
	global_store_dword v[16:17], v20, off sc1
.LBB0_1413:
	s_or_b64 exec, exec, s[20:21]
	s_waitcnt vmcnt(5)
	v_lshlrev_b32_e32 v20, 16, v52
	v_and_b32_e32 v21, 0xffff0000, v52
	v_lshlrev_b32_e32 v22, 16, v53
	v_and_b32_e32 v23, 0xffff0000, v53
	v_pk_fma_f32 v[14:15], v[14:15], v[110:111], v[22:23]
	v_pk_fma_f32 v[12:13], v[12:13], v[108:109], v[20:21]
	v_mul_f32_e32 v21, v15, v15
	v_mul_f32_e32 v20, v13, v13
	v_fmac_f32_e32 v20, v12, v12
	v_fmac_f32_e32 v21, v14, v14
	v_add_f32_e32 v22, v20, v21
	v_cvt_pk_bf16_f32 v12, v12, v13
	v_cvt_pk_bf16_f32 v13, v14, v15
	v_lshlrev_b32_e32 v14, 16, v54
	v_and_b32_e32 v15, 0xffff0000, v54
	v_lshlrev_b32_e32 v20, 16, v55
	v_and_b32_e32 v21, 0xffff0000, v55
	v_pk_fma_f32 v[10:11], v[10:11], v[102:103], v[20:21]
	v_pk_fma_f32 v[8:9], v[8:9], v[100:101], v[14:15]
	v_mul_f32_e32 v15, v11, v11
	v_mul_f32_e32 v14, v9, v9
	v_fmac_f32_e32 v14, v8, v8
	v_fmac_f32_e32 v15, v10, v10
	v_add_f32_e32 v14, v14, v15
	v_add_f32_e32 v22, v22, v14
	s_waitcnt vmcnt(4)
	v_lshlrev_b32_e32 v14, 16, v48
	v_and_b32_e32 v15, 0xffff0000, v48
	v_lshlrev_b32_e32 v20, 16, v49
	v_and_b32_e32 v21, 0xffff0000, v49
	v_pk_fma_f32 v[6:7], v[6:7], v[94:95], v[20:21]
	v_pk_fma_f32 v[4:5], v[4:5], v[92:93], v[14:15]
	v_mul_f32_e32 v15, v7, v7
	v_mul_f32_e32 v14, v5, v5
	v_fmac_f32_e32 v14, v4, v4
	v_fmac_f32_e32 v15, v6, v6
	v_add_f32_e32 v14, v14, v15
	v_add_f32_e32 v24, v22, v14
	v_lshlrev_b32_e32 v14, 16, v50
	v_and_b32_e32 v15, 0xffff0000, v50
	v_lshlrev_b32_e32 v20, 16, v51
	v_and_b32_e32 v21, 0xffff0000, v51
	v_pk_fma_f32 v[20:21], v[2:3], v[90:91], v[20:21]
	v_pk_fma_f32 v[22:23], v[0:1], v[88:89], v[14:15]
	v_mul_f32_e32 v1, v21, v21
	v_mul_f32_e32 v0, v23, v23
	v_fmac_f32_e32 v0, v22, v22
	v_fmac_f32_e32 v1, v20, v20
	v_add_f32_e32 v0, v0, v1
	v_add_f32_e32 v0, v0, v24
	ds_bpermute_b32 v1, v128, v0
	s_mov_b64 s[20:21], 0x5800
	s_waitcnt lgkmcnt(1)
	v_lshl_add_u64 v[16:17], v[188:189], 0, s[20:21]
	s_mov_b64 s[20:21], 0x15800
	v_lshl_add_u64 v[18:19], v[188:189], 0, s[20:21]
	s_waitcnt lgkmcnt(0)
	v_add_f32_e32 v0, v0, v1
	ds_bpermute_b32 v1, v196, v0
	v_cvt_pk_bf16_f32 v14, v8, v9
	v_cvt_pk_bf16_f32 v15, v10, v11
	v_cvt_pk_bf16_f32 v2, v4, v5
	v_cvt_pk_bf16_f32 v3, v6, v7
	v_cvt_pk_bf16_f32 v4, v22, v23
	v_cvt_pk_bf16_f32 v5, v20, v21
	global_store_dwordx4 v[16:17], v[12:15], off sc1
	global_store_dwordx4 v[18:19], v[2:5], off sc1
	s_and_saveexec_b64 s[20:21], s[4:5]
	s_cbranch_execz .LBB0_1415
	v_or_b32_e32 v2, 48, v72
	v_ashrrev_i32_e32 v3, 31, v2
	s_waitcnt lgkmcnt(0)
	v_add_f32_e32 v4, v0, v1
	v_lshlrev_b64 v[0:1], 7, v[2:3]
	v_lshl_add_u64 v[0:1], s[12:13], 0, v[0:1]
	v_lshl_add_u64 v[0:1], s[18:19], 2, v[0:1]
	s_lshl_b32 s64, s36, 2
	v_lshl_add_u64 v[0:1], v[0:1], 0, s[64:65]
	global_store_dword v[0:1], v4, off sc1
